# attn kernel MLP-weight conversion path rewritten: one wave per 64x64 tile, 4 tiles per block, wave-private LDS, no block barrier
# baseline (speedup 1.0000x reference)
.LBB2_27:
	s_and_b64 vcc, exec, s[4:5]
	s_cbranch_vccz .LBB2_43
	s_branch .Lcv_start

.Lcv_start:
	s_addk_i32 s2, 0xfda8
	s_cmpk_lt_u32 s2, 0x120
	s_cbranch_scc0 .LBB2_43
	s_load_dwordx4 s[8:11], s[0:1], 0x30
	s_load_dwordx4 s[12:15], s[0:1], 0x50
	s_load_dwordx8 s[16:23], s[0:1], 0xb0
	v_lshrrev_b32_e32 v1, 6, v0
	v_and_b32_e32 v0, 63, v0
	v_readfirstlane_b32 s3, v1
	s_nop 3
	s_lshl_b32 s2, s2, 2
	s_add_u32 s2, s2, s3
	s_mul_i32 s24, s3, 0x4100
	s_cmpk_ge_u32 s2, 0x240
	s_cbranch_scc1 .Lcv_w2
	s_lshr_b32 s4, s2, 4
	s_mul_i32 s4, s4, 0xaaab
	s_lshr_b32 s4, s4, 17
	s_mul_i32 s5, s4, 48
	s_sub_u32 s5, s2, s5
	s_movk_i32 s6, 0x300
	s_movk_i32 s7, 0xc00
	s_mov_b32 s25, 1
	s_waitcnt lgkmcnt(0)
	s_mov_b64 s[26:27], s[8:9]
	s_mov_b64 s[28:29], s[12:13]
	s_branch .Lcv_common
.Lcv_w2:
	s_sub_u32 s2, s2, 0x240
	s_lshr_b32 s4, s2, 2
	s_mul_i32 s4, s4, 0xaaab
	s_lshr_b32 s4, s4, 17
	s_mul_i32 s5, s4, 12
	s_sub_u32 s5, s2, s5
	s_movk_i32 s6, 0xc00
	s_movk_i32 s7, 0x300
	s_mov_b32 s25, 0
	s_waitcnt lgkmcnt(0)
	s_mov_b64 s[26:27], s[10:11]
	s_mov_b64 s[28:29], s[14:15]
.Lcv_common:
	s_lshl_b32 s4, s4, 6
	s_lshl_b32 s5, s5, 6
	s_mul_i32 s30, s4, s7
	s_add_u32 s30, s30, s5
	s_lshl_b32 s30, s30, 2
	s_add_u32 s26, s26, s30
	s_addc_u32 s27, s27, 0
	s_lshl_b32 s31, s7, 4
	s_mul_i32 s30, s5, s6
	s_add_u32 s30, s30, s4
	s_lshl_b32 s30, s30, 1
	s_add_u32 s28, s28, s30
	s_addc_u32 s29, s29, 0
	s_lshl_b32 s33, s6, 4
	v_lshrrev_b32_e32 v2, 4, v0
	v_and_b32_e32 v3, 15, v0
	v_mul_lo_u32 v4, v2, s7
	v_lshlrev_b32_e32 v4, 2, v4
	v_lshl_add_u32 v4, v3, 4, v4
	v_mul_u32_u24_e32 v5, 0x104, v2
	v_lshl_add_u32 v5, v3, 4, v5
	v_add_u32_e32 v5, s24, v5
	v_and_b32_e32 v6, 7, v0
	v_lshrrev_b32_e32 v7, 3, v0
	v_mul_u32_u24_e32 v8, 0x820, v7
	v_lshl_add_u32 v8, v6, 2, v8
	v_add_u32_e32 v8, s24, v8
	v_mul_lo_u32 v9, v6, s6
	v_lshl_add_u32 v9, v7, 3, v9
	v_lshlrev_b32_e32 v9, 1, v9
	v_lshl_add_u32 v10, v0, 2, s24
	v_mov_b32_e32 v80, 1.0
	v_mov_b32_e32 v81, 1.0
	v_mov_b32_e32 v82, 1.0
	v_mov_b32_e32 v83, 1.0
	v_mov_b32_e32 v84, 1.0
	v_mov_b32_e32 v85, 1.0
	v_mov_b32_e32 v86, 1.0
	v_mov_b32_e32 v87, 1.0
	s_cmp_eq_u32 s25, 0
	s_cbranch_scc1 .Lcv_nogain
	s_lshl_b32 s30, s4, 2
	s_add_u32 s16, s16, s30
	s_addc_u32 s17, s17, 0
	s_add_u32 s18, s18, s30
	s_addc_u32 s19, s19, 0
	v_lshlrev_b32_e32 v11, 5, v7
	global_load_dwordx4 v[80:83], v11, s[16:17]
	global_load_dwordx4 v[84:87], v11, s[16:17] offset:16
	s_load_dwordx16 s[36:51], s[16:17], 0x0
	s_load_dwordx16 s[52:67], s[16:17], 0x40
	s_load_dwordx16 s[68:83], s[18:19], 0x0
	s_load_dwordx16 s[84:99], s[18:19], 0x40
.Lcv_nogain:
	global_load_dwordx4 v[16:19], v4, s[26:27] nt
	s_add_u32 s26, s26, s31
	s_addc_u32 s27, s27, 0
	global_load_dwordx4 v[20:23], v4, s[26:27] nt
	s_add_u32 s26, s26, s31
	s_addc_u32 s27, s27, 0
	global_load_dwordx4 v[24:27], v4, s[26:27] nt
	s_add_u32 s26, s26, s31
	s_addc_u32 s27, s27, 0
	global_load_dwordx4 v[28:31], v4, s[26:27] nt
	s_add_u32 s26, s26, s31
	s_addc_u32 s27, s27, 0
	global_load_dwordx4 v[32:35], v4, s[26:27] nt
	s_add_u32 s26, s26, s31
	s_addc_u32 s27, s27, 0
	global_load_dwordx4 v[36:39], v4, s[26:27] nt
	s_add_u32 s26, s26, s31
	s_addc_u32 s27, s27, 0
	global_load_dwordx4 v[40:43], v4, s[26:27] nt
	s_add_u32 s26, s26, s31
	s_addc_u32 s27, s27, 0
	global_load_dwordx4 v[44:47], v4, s[26:27] nt
	s_add_u32 s26, s26, s31
	s_addc_u32 s27, s27, 0
	global_load_dwordx4 v[48:51], v4, s[26:27] nt
	s_add_u32 s26, s26, s31
	s_addc_u32 s27, s27, 0
	global_load_dwordx4 v[52:55], v4, s[26:27] nt
	s_add_u32 s26, s26, s31
	s_addc_u32 s27, s27, 0
	global_load_dwordx4 v[56:59], v4, s[26:27] nt
	s_add_u32 s26, s26, s31
	s_addc_u32 s27, s27, 0
	global_load_dwordx4 v[60:63], v4, s[26:27] nt
	s_add_u32 s26, s26, s31
	s_addc_u32 s27, s27, 0
	global_load_dwordx4 v[64:67], v4, s[26:27] nt
	s_add_u32 s26, s26, s31
	s_addc_u32 s27, s27, 0
	global_load_dwordx4 v[68:71], v4, s[26:27] nt
	s_add_u32 s26, s26, s31
	s_addc_u32 s27, s27, 0
	global_load_dwordx4 v[72:75], v4, s[26:27] nt
	s_add_u32 s26, s26, s31
	s_addc_u32 s27, s27, 0
	global_load_dwordx4 v[76:79], v4, s[26:27] nt
	s_waitcnt vmcnt(15)
	ds_write_b32 v5, v16 offset:0
	ds_write_b32 v5, v17 offset:4
	ds_write_b32 v5, v18 offset:8
	ds_write_b32 v5, v19 offset:12
	s_waitcnt vmcnt(14)
	ds_write_b32 v5, v20 offset:1040
	ds_write_b32 v5, v21 offset:1044
	ds_write_b32 v5, v22 offset:1048
	ds_write_b32 v5, v23 offset:1052
	s_waitcnt vmcnt(13)
	ds_write_b32 v5, v24 offset:2080
	ds_write_b32 v5, v25 offset:2084
	ds_write_b32 v5, v26 offset:2088
	ds_write_b32 v5, v27 offset:2092
	s_waitcnt vmcnt(12)
	ds_write_b32 v5, v28 offset:3120
	ds_write_b32 v5, v29 offset:3124
	ds_write_b32 v5, v30 offset:3128
	ds_write_b32 v5, v31 offset:3132
	s_waitcnt vmcnt(11)
	ds_write_b32 v5, v32 offset:4160
	ds_write_b32 v5, v33 offset:4164
	ds_write_b32 v5, v34 offset:4168
	ds_write_b32 v5, v35 offset:4172
	s_waitcnt vmcnt(10)
	ds_write_b32 v5, v36 offset:5200
	ds_write_b32 v5, v37 offset:5204
	ds_write_b32 v5, v38 offset:5208
	ds_write_b32 v5, v39 offset:5212
	s_waitcnt vmcnt(9)
	ds_write_b32 v5, v40 offset:6240
	ds_write_b32 v5, v41 offset:6244
	ds_write_b32 v5, v42 offset:6248
	ds_write_b32 v5, v43 offset:6252
	s_waitcnt vmcnt(8)
	ds_write_b32 v5, v44 offset:7280
	ds_write_b32 v5, v45 offset:7284
	ds_write_b32 v5, v46 offset:7288
	ds_write_b32 v5, v47 offset:7292
	s_waitcnt vmcnt(7)
	ds_write_b32 v5, v48 offset:8320
	ds_write_b32 v5, v49 offset:8324
	ds_write_b32 v5, v50 offset:8328
	ds_write_b32 v5, v51 offset:8332
	s_waitcnt vmcnt(6)
	ds_write_b32 v5, v52 offset:9360
	ds_write_b32 v5, v53 offset:9364
	ds_write_b32 v5, v54 offset:9368
	ds_write_b32 v5, v55 offset:9372
	s_waitcnt vmcnt(5)
	ds_write_b32 v5, v56 offset:10400
	ds_write_b32 v5, v57 offset:10404
	ds_write_b32 v5, v58 offset:10408
	ds_write_b32 v5, v59 offset:10412
	s_waitcnt vmcnt(4)
	ds_write_b32 v5, v60 offset:11440
	ds_write_b32 v5, v61 offset:11444
	ds_write_b32 v5, v62 offset:11448
	ds_write_b32 v5, v63 offset:11452
	s_waitcnt vmcnt(3)
	ds_write_b32 v5, v64 offset:12480
	ds_write_b32 v5, v65 offset:12484
	ds_write_b32 v5, v66 offset:12488
	ds_write_b32 v5, v67 offset:12492
	s_waitcnt vmcnt(2)
	ds_write_b32 v5, v68 offset:13520
	ds_write_b32 v5, v69 offset:13524
	ds_write_b32 v5, v70 offset:13528
	ds_write_b32 v5, v71 offset:13532
	s_waitcnt vmcnt(1)
	ds_write_b32 v5, v72 offset:14560
	ds_write_b32 v5, v73 offset:14564
	ds_write_b32 v5, v74 offset:14568
	ds_write_b32 v5, v75 offset:14572
	s_waitcnt vmcnt(0)
	ds_write_b32 v5, v76 offset:15600
	ds_write_b32 v5, v77 offset:15604
	ds_write_b32 v5, v78 offset:15608
	ds_write_b32 v5, v79 offset:15612
	s_waitcnt lgkmcnt(0)
	ds_read_b32 v88, v8 offset:0
	ds_read_b32 v89, v8 offset:260
	ds_read_b32 v90, v8 offset:520
	ds_read_b32 v91, v8 offset:780
	ds_read_b32 v92, v8 offset:1040
	ds_read_b32 v93, v8 offset:1300
	ds_read_b32 v94, v8 offset:1560
	ds_read_b32 v95, v8 offset:1820
	s_waitcnt lgkmcnt(0)
	v_pk_mul_f32 v[88:89], v[88:89], v[80:81]
	v_pk_mul_f32 v[90:91], v[90:91], v[82:83]
	v_pk_mul_f32 v[92:93], v[92:93], v[84:85]
	v_pk_mul_f32 v[94:95], v[94:95], v[86:87]
	v_cvt_pk_f16_f32 v104, v88, v89
	v_cvt_pk_f16_f32 v105, v90, v91
	v_cvt_pk_f16_f32 v106, v92, v93
	v_cvt_pk_f16_f32 v107, v94, v95
	global_store_dwordx4 v9, v[104:107], s[28:29]
	s_add_u32 s28, s28, s33
	s_addc_u32 s29, s29, 0
	ds_read_b32 v96, v8 offset:32
	ds_read_b32 v97, v8 offset:292
	ds_read_b32 v98, v8 offset:552
	ds_read_b32 v99, v8 offset:812
	ds_read_b32 v100, v8 offset:1072
	ds_read_b32 v101, v8 offset:1332
	ds_read_b32 v102, v8 offset:1592
	ds_read_b32 v103, v8 offset:1852
	s_waitcnt lgkmcnt(0)
	v_pk_mul_f32 v[96:97], v[96:97], v[80:81]
	v_pk_mul_f32 v[98:99], v[98:99], v[82:83]
	v_pk_mul_f32 v[100:101], v[100:101], v[84:85]
	v_pk_mul_f32 v[102:103], v[102:103], v[86:87]
	v_cvt_pk_f16_f32 v108, v96, v97
	v_cvt_pk_f16_f32 v109, v98, v99
	v_cvt_pk_f16_f32 v110, v100, v101
	v_cvt_pk_f16_f32 v111, v102, v103
	global_store_dwordx4 v9, v[108:111], s[28:29]
	s_add_u32 s28, s28, s33
	s_addc_u32 s29, s29, 0
	ds_read_b32 v88, v8 offset:64
	ds_read_b32 v89, v8 offset:324
	ds_read_b32 v90, v8 offset:584
	ds_read_b32 v91, v8 offset:844
	ds_read_b32 v92, v8 offset:1104
	ds_read_b32 v93, v8 offset:1364
	ds_read_b32 v94, v8 offset:1624
	ds_read_b32 v95, v8 offset:1884
	s_waitcnt lgkmcnt(0)
	v_pk_mul_f32 v[88:89], v[88:89], v[80:81]
	v_pk_mul_f32 v[90:91], v[90:91], v[82:83]
	v_pk_mul_f32 v[92:93], v[92:93], v[84:85]
	v_pk_mul_f32 v[94:95], v[94:95], v[86:87]
	v_cvt_pk_f16_f32 v112, v88, v89
	v_cvt_pk_f16_f32 v113, v90, v91
	v_cvt_pk_f16_f32 v114, v92, v93
	v_cvt_pk_f16_f32 v115, v94, v95
	global_store_dwordx4 v9, v[112:115], s[28:29]
	s_add_u32 s28, s28, s33
	s_addc_u32 s29, s29, 0
	ds_read_b32 v96, v8 offset:96
	ds_read_b32 v97, v8 offset:356
	ds_read_b32 v98, v8 offset:616
	ds_read_b32 v99, v8 offset:876
	ds_read_b32 v100, v8 offset:1136
	ds_read_b32 v101, v8 offset:1396
	ds_read_b32 v102, v8 offset:1656
	ds_read_b32 v103, v8 offset:1916
	s_waitcnt lgkmcnt(0)
	v_pk_mul_f32 v[96:97], v[96:97], v[80:81]
	v_pk_mul_f32 v[98:99], v[98:99], v[82:83]
	v_pk_mul_f32 v[100:101], v[100:101], v[84:85]
	v_pk_mul_f32 v[102:103], v[102:103], v[86:87]
	v_cvt_pk_f16_f32 v116, v96, v97
	v_cvt_pk_f16_f32 v117, v98, v99
	v_cvt_pk_f16_f32 v118, v100, v101
	v_cvt_pk_f16_f32 v119, v102, v103
	global_store_dwordx4 v9, v[116:119], s[28:29]
	s_add_u32 s28, s28, s33
	s_addc_u32 s29, s29, 0
	ds_read_b32 v88, v8 offset:128
	ds_read_b32 v89, v8 offset:388
	ds_read_b32 v90, v8 offset:648
	ds_read_b32 v91, v8 offset:908
	ds_read_b32 v92, v8 offset:1168
	ds_read_b32 v93, v8 offset:1428
	ds_read_b32 v94, v8 offset:1688
	ds_read_b32 v95, v8 offset:1948
	s_waitcnt lgkmcnt(0)
	v_pk_mul_f32 v[88:89], v[88:89], v[80:81]
	v_pk_mul_f32 v[90:91], v[90:91], v[82:83]
	v_pk_mul_f32 v[92:93], v[92:93], v[84:85]
	v_pk_mul_f32 v[94:95], v[94:95], v[86:87]
	v_cvt_pk_f16_f32 v104, v88, v89
	v_cvt_pk_f16_f32 v105, v90, v91
	v_cvt_pk_f16_f32 v106, v92, v93
	v_cvt_pk_f16_f32 v107, v94, v95
	global_store_dwordx4 v9, v[104:107], s[28:29]
	s_add_u32 s28, s28, s33
	s_addc_u32 s29, s29, 0
	ds_read_b32 v96, v8 offset:160
	ds_read_b32 v97, v8 offset:420
	ds_read_b32 v98, v8 offset:680
	ds_read_b32 v99, v8 offset:940
	ds_read_b32 v100, v8 offset:1200
	ds_read_b32 v101, v8 offset:1460
	ds_read_b32 v102, v8 offset:1720
	ds_read_b32 v103, v8 offset:1980
	s_waitcnt lgkmcnt(0)
	v_pk_mul_f32 v[96:97], v[96:97], v[80:81]
	v_pk_mul_f32 v[98:99], v[98:99], v[82:83]
	v_pk_mul_f32 v[100:101], v[100:101], v[84:85]
	v_pk_mul_f32 v[102:103], v[102:103], v[86:87]
	v_cvt_pk_f16_f32 v108, v96, v97
	v_cvt_pk_f16_f32 v109, v98, v99
	v_cvt_pk_f16_f32 v110, v100, v101
	v_cvt_pk_f16_f32 v111, v102, v103
	global_store_dwordx4 v9, v[108:111], s[28:29]
	s_add_u32 s28, s28, s33
	s_addc_u32 s29, s29, 0
	ds_read_b32 v88, v8 offset:192
	ds_read_b32 v89, v8 offset:452
	ds_read_b32 v90, v8 offset:712
	ds_read_b32 v91, v8 offset:972
	ds_read_b32 v92, v8 offset:1232
	ds_read_b32 v93, v8 offset:1492
	ds_read_b32 v94, v8 offset:1752
	ds_read_b32 v95, v8 offset:2012
	s_waitcnt lgkmcnt(0)
	v_pk_mul_f32 v[88:89], v[88:89], v[80:81]
	v_pk_mul_f32 v[90:91], v[90:91], v[82:83]
	v_pk_mul_f32 v[92:93], v[92:93], v[84:85]
	v_pk_mul_f32 v[94:95], v[94:95], v[86:87]
	v_cvt_pk_f16_f32 v112, v88, v89
	v_cvt_pk_f16_f32 v113, v90, v91
	v_cvt_pk_f16_f32 v114, v92, v93
	v_cvt_pk_f16_f32 v115, v94, v95
	global_store_dwordx4 v9, v[112:115], s[28:29]
	s_add_u32 s28, s28, s33
	s_addc_u32 s29, s29, 0
	ds_read_b32 v96, v8 offset:224
	ds_read_b32 v97, v8 offset:484
	ds_read_b32 v98, v8 offset:744
	ds_read_b32 v99, v8 offset:1004
	ds_read_b32 v100, v8 offset:1264
	ds_read_b32 v101, v8 offset:1524
	ds_read_b32 v102, v8 offset:1784
	ds_read_b32 v103, v8 offset:2044
	s_waitcnt lgkmcnt(0)
	v_pk_mul_f32 v[96:97], v[96:97], v[80:81]
	v_pk_mul_f32 v[98:99], v[98:99], v[82:83]
	v_pk_mul_f32 v[100:101], v[100:101], v[84:85]
	v_pk_mul_f32 v[102:103], v[102:103], v[86:87]
	v_cvt_pk_f16_f32 v116, v96, v97
	v_cvt_pk_f16_f32 v117, v98, v99
	v_cvt_pk_f16_f32 v118, v100, v101
	v_cvt_pk_f16_f32 v119, v102, v103
	global_store_dwordx4 v9, v[116:119], s[28:29]
	s_cmp_eq_u32 s25, 0
	s_cbranch_scc1 .LBB2_43
	v_mov_b32_e32 v12, 0
	v_mov_b32_e32 v13, 0
	ds_read_b32 v112, v10 offset:0
	ds_read_b32 v113, v10 offset:260
	ds_read_b32 v114, v10 offset:520
	ds_read_b32 v115, v10 offset:780
	ds_read_b32 v116, v10 offset:1040
	ds_read_b32 v117, v10 offset:1300
	ds_read_b32 v118, v10 offset:1560
	ds_read_b32 v119, v10 offset:1820
	ds_read_b32 v120, v10 offset:2080
	ds_read_b32 v121, v10 offset:2340
	ds_read_b32 v122, v10 offset:2600
	ds_read_b32 v123, v10 offset:2860
	ds_read_b32 v124, v10 offset:3120
	ds_read_b32 v125, v10 offset:3380
	ds_read_b32 v126, v10 offset:3640
	ds_read_b32 v127, v10 offset:3900
	s_waitcnt lgkmcnt(0)
	v_mul_f32_e32 v128, s36, v112
	v_fmac_f32_e32 v13, s68, v112
	v_cvt_f16_f32_e32 v128, v128
	v_cvt_f32_f16_e32 v128, v128
	v_add_f32_e32 v12, v12, v128
	v_mul_f32_e32 v129, s37, v113
	v_fmac_f32_e32 v13, s69, v113
	v_cvt_f16_f32_e32 v129, v129
	v_cvt_f32_f16_e32 v129, v129
	v_add_f32_e32 v12, v12, v129
	v_mul_f32_e32 v130, s38, v114
	v_fmac_f32_e32 v13, s70, v114
	v_cvt_f16_f32_e32 v130, v130
	v_cvt_f32_f16_e32 v130, v130
	v_add_f32_e32 v12, v12, v130
	v_mul_f32_e32 v131, s39, v115
	v_fmac_f32_e32 v13, s71, v115
	v_cvt_f16_f32_e32 v131, v131
	v_cvt_f32_f16_e32 v131, v131
	v_add_f32_e32 v12, v12, v131
	v_mul_f32_e32 v128, s40, v116
	v_fmac_f32_e32 v13, s72, v116
	v_cvt_f16_f32_e32 v128, v128
	v_cvt_f32_f16_e32 v128, v128
	v_add_f32_e32 v12, v12, v128
	v_mul_f32_e32 v129, s41, v117
	v_fmac_f32_e32 v13, s73, v117
	v_cvt_f16_f32_e32 v129, v129
	v_cvt_f32_f16_e32 v129, v129
	v_add_f32_e32 v12, v12, v129
	v_mul_f32_e32 v130, s42, v118
	v_fmac_f32_e32 v13, s74, v118
	v_cvt_f16_f32_e32 v130, v130
	v_cvt_f32_f16_e32 v130, v130
	v_add_f32_e32 v12, v12, v130
	v_mul_f32_e32 v131, s43, v119
	v_fmac_f32_e32 v13, s75, v119
	v_cvt_f16_f32_e32 v131, v131
	v_cvt_f32_f16_e32 v131, v131
	v_add_f32_e32 v12, v12, v131
	v_mul_f32_e32 v128, s44, v120
	v_fmac_f32_e32 v13, s76, v120
	v_cvt_f16_f32_e32 v128, v128
	v_cvt_f32_f16_e32 v128, v128
	v_add_f32_e32 v12, v12, v128
	v_mul_f32_e32 v129, s45, v121
	v_fmac_f32_e32 v13, s77, v121
	v_cvt_f16_f32_e32 v129, v129
	v_cvt_f32_f16_e32 v129, v129
	v_add_f32_e32 v12, v12, v129
	v_mul_f32_e32 v130, s46, v122
	v_fmac_f32_e32 v13, s78, v122
	v_cvt_f16_f32_e32 v130, v130
	v_cvt_f32_f16_e32 v130, v130
	v_add_f32_e32 v12, v12, v130
	v_mul_f32_e32 v131, s47, v123
	v_fmac_f32_e32 v13, s79, v123
	v_cvt_f16_f32_e32 v131, v131
	v_cvt_f32_f16_e32 v131, v131
	v_add_f32_e32 v12, v12, v131
	v_mul_f32_e32 v128, s48, v124
	v_fmac_f32_e32 v13, s80, v124
	v_cvt_f16_f32_e32 v128, v128
	v_cvt_f32_f16_e32 v128, v128
	v_add_f32_e32 v12, v12, v128
	v_mul_f32_e32 v129, s49, v125
	v_fmac_f32_e32 v13, s81, v125
	v_cvt_f16_f32_e32 v129, v129
	v_cvt_f32_f16_e32 v129, v129
	v_add_f32_e32 v12, v12, v129
	v_mul_f32_e32 v130, s50, v126
	v_fmac_f32_e32 v13, s82, v126
	v_cvt_f16_f32_e32 v130, v130
	v_cvt_f32_f16_e32 v130, v130
	v_add_f32_e32 v12, v12, v130
	v_mul_f32_e32 v131, s51, v127
	v_fmac_f32_e32 v13, s83, v127
	v_cvt_f16_f32_e32 v131, v131
	v_cvt_f32_f16_e32 v131, v131
	v_add_f32_e32 v12, v12, v131
	ds_read_b32 v112, v10 offset:4160
	ds_read_b32 v113, v10 offset:4420
	ds_read_b32 v114, v10 offset:4680
	ds_read_b32 v115, v10 offset:4940
	ds_read_b32 v116, v10 offset:5200
	ds_read_b32 v117, v10 offset:5460
	ds_read_b32 v118, v10 offset:5720
	ds_read_b32 v119, v10 offset:5980
	ds_read_b32 v120, v10 offset:6240
	ds_read_b32 v121, v10 offset:6500
	ds_read_b32 v122, v10 offset:6760
	ds_read_b32 v123, v10 offset:7020
	ds_read_b32 v124, v10 offset:7280
	ds_read_b32 v125, v10 offset:7540
	ds_read_b32 v126, v10 offset:7800
	ds_read_b32 v127, v10 offset:8060
	s_waitcnt lgkmcnt(0)
	v_mul_f32_e32 v128, s52, v112
	v_fmac_f32_e32 v13, s84, v112
	v_cvt_f16_f32_e32 v128, v128
	v_cvt_f32_f16_e32 v128, v128
	v_add_f32_e32 v12, v12, v128
	v_mul_f32_e32 v129, s53, v113
	v_fmac_f32_e32 v13, s85, v113
	v_cvt_f16_f32_e32 v129, v129
	v_cvt_f32_f16_e32 v129, v129
	v_add_f32_e32 v12, v12, v129
	v_mul_f32_e32 v130, s54, v114
	v_fmac_f32_e32 v13, s86, v114
	v_cvt_f16_f32_e32 v130, v130
	v_cvt_f32_f16_e32 v130, v130
	v_add_f32_e32 v12, v12, v130
	v_mul_f32_e32 v131, s55, v115
	v_fmac_f32_e32 v13, s87, v115
	v_cvt_f16_f32_e32 v131, v131
	v_cvt_f32_f16_e32 v131, v131
	v_add_f32_e32 v12, v12, v131
	v_mul_f32_e32 v128, s56, v116
	v_fmac_f32_e32 v13, s88, v116
	v_cvt_f16_f32_e32 v128, v128
	v_cvt_f32_f16_e32 v128, v128
	v_add_f32_e32 v12, v12, v128
	v_mul_f32_e32 v129, s57, v117
	v_fmac_f32_e32 v13, s89, v117
	v_cvt_f16_f32_e32 v129, v129
	v_cvt_f32_f16_e32 v129, v129
	v_add_f32_e32 v12, v12, v129
	v_mul_f32_e32 v130, s58, v118
	v_fmac_f32_e32 v13, s90, v118
	v_cvt_f16_f32_e32 v130, v130
	v_cvt_f32_f16_e32 v130, v130
	v_add_f32_e32 v12, v12, v130
	v_mul_f32_e32 v131, s59, v119
	v_fmac_f32_e32 v13, s91, v119
	v_cvt_f16_f32_e32 v131, v131
	v_cvt_f32_f16_e32 v131, v131
	v_add_f32_e32 v12, v12, v131
	v_mul_f32_e32 v128, s60, v120
	v_fmac_f32_e32 v13, s92, v120
	v_cvt_f16_f32_e32 v128, v128
	v_cvt_f32_f16_e32 v128, v128
	v_add_f32_e32 v12, v12, v128
	v_mul_f32_e32 v129, s61, v121
	v_fmac_f32_e32 v13, s93, v121
	v_cvt_f16_f32_e32 v129, v129
	v_cvt_f32_f16_e32 v129, v129
	v_add_f32_e32 v12, v12, v129
	v_mul_f32_e32 v130, s62, v122
	v_fmac_f32_e32 v13, s94, v122
	v_cvt_f16_f32_e32 v130, v130
	v_cvt_f32_f16_e32 v130, v130
	v_add_f32_e32 v12, v12, v130
	v_mul_f32_e32 v131, s63, v123
	v_fmac_f32_e32 v13, s95, v123
	v_cvt_f16_f32_e32 v131, v131
	v_cvt_f32_f16_e32 v131, v131
	v_add_f32_e32 v12, v12, v131
	v_mul_f32_e32 v128, s64, v124
	v_fmac_f32_e32 v13, s96, v124
	v_cvt_f16_f32_e32 v128, v128
	v_cvt_f32_f16_e32 v128, v128
	v_add_f32_e32 v12, v12, v128
	v_mul_f32_e32 v129, s65, v125
	v_fmac_f32_e32 v13, s97, v125
	v_cvt_f16_f32_e32 v129, v129
	v_cvt_f32_f16_e32 v129, v129
	v_add_f32_e32 v12, v12, v129
	v_mul_f32_e32 v130, s66, v126
	v_fmac_f32_e32 v13, s98, v126
	v_cvt_f16_f32_e32 v130, v130
	v_cvt_f32_f16_e32 v130, v130
	v_add_f32_e32 v12, v12, v130
	v_mul_f32_e32 v131, s67, v127
	v_fmac_f32_e32 v13, s99, v127
	v_cvt_f16_f32_e32 v131, v131
	v_cvt_f32_f16_e32 v131, v131
	v_add_f32_e32 v12, v12, v131
	s_load_dwordx16 s[36:51], s[16:17], 0x80
	s_load_dwordx16 s[52:67], s[16:17], 0xc0
	s_load_dwordx16 s[68:83], s[18:19], 0x80
	s_load_dwordx16 s[84:99], s[18:19], 0xc0
	ds_read_b32 v112, v10 offset:8320
	ds_read_b32 v113, v10 offset:8580
	ds_read_b32 v114, v10 offset:8840
	ds_read_b32 v115, v10 offset:9100
	ds_read_b32 v116, v10 offset:9360
	ds_read_b32 v117, v10 offset:9620
	ds_read_b32 v118, v10 offset:9880
	ds_read_b32 v119, v10 offset:10140
	ds_read_b32 v120, v10 offset:10400
	ds_read_b32 v121, v10 offset:10660
	ds_read_b32 v122, v10 offset:10920
	ds_read_b32 v123, v10 offset:11180
	ds_read_b32 v124, v10 offset:11440
	ds_read_b32 v125, v10 offset:11700
	ds_read_b32 v126, v10 offset:11960
	ds_read_b32 v127, v10 offset:12220
	s_waitcnt lgkmcnt(0)
	v_mul_f32_e32 v128, s36, v112
	v_fmac_f32_e32 v13, s68, v112
	v_cvt_f16_f32_e32 v128, v128
	v_cvt_f32_f16_e32 v128, v128
	v_add_f32_e32 v12, v12, v128
	v_mul_f32_e32 v129, s37, v113
	v_fmac_f32_e32 v13, s69, v113
	v_cvt_f16_f32_e32 v129, v129
	v_cvt_f32_f16_e32 v129, v129
	v_add_f32_e32 v12, v12, v129
	v_mul_f32_e32 v130, s38, v114
	v_fmac_f32_e32 v13, s70, v114
	v_cvt_f16_f32_e32 v130, v130
	v_cvt_f32_f16_e32 v130, v130
	v_add_f32_e32 v12, v12, v130
	v_mul_f32_e32 v131, s39, v115
	v_fmac_f32_e32 v13, s71, v115
	v_cvt_f16_f32_e32 v131, v131
	v_cvt_f32_f16_e32 v131, v131
	v_add_f32_e32 v12, v12, v131
	v_mul_f32_e32 v128, s40, v116
	v_fmac_f32_e32 v13, s72, v116
	v_cvt_f16_f32_e32 v128, v128
	v_cvt_f32_f16_e32 v128, v128
	v_add_f32_e32 v12, v12, v128
	v_mul_f32_e32 v129, s41, v117
	v_fmac_f32_e32 v13, s73, v117
	v_cvt_f16_f32_e32 v129, v129
	v_cvt_f32_f16_e32 v129, v129
	v_add_f32_e32 v12, v12, v129
	v_mul_f32_e32 v130, s42, v118
	v_fmac_f32_e32 v13, s74, v118
	v_cvt_f16_f32_e32 v130, v130
	v_cvt_f32_f16_e32 v130, v130
	v_add_f32_e32 v12, v12, v130
	v_mul_f32_e32 v131, s43, v119
	v_fmac_f32_e32 v13, s75, v119
	v_cvt_f16_f32_e32 v131, v131
	v_cvt_f32_f16_e32 v131, v131
	v_add_f32_e32 v12, v12, v131
	v_mul_f32_e32 v128, s44, v120
	v_fmac_f32_e32 v13, s76, v120
	v_cvt_f16_f32_e32 v128, v128
	v_cvt_f32_f16_e32 v128, v128
	v_add_f32_e32 v12, v12, v128
	v_mul_f32_e32 v129, s45, v121
	v_fmac_f32_e32 v13, s77, v121
	v_cvt_f16_f32_e32 v129, v129
	v_cvt_f32_f16_e32 v129, v129
	v_add_f32_e32 v12, v12, v129
	v_mul_f32_e32 v130, s46, v122
	v_fmac_f32_e32 v13, s78, v122
	v_cvt_f16_f32_e32 v130, v130
	v_cvt_f32_f16_e32 v130, v130
	v_add_f32_e32 v12, v12, v130
	v_mul_f32_e32 v131, s47, v123
	v_fmac_f32_e32 v13, s79, v123
	v_cvt_f16_f32_e32 v131, v131
	v_cvt_f32_f16_e32 v131, v131
	v_add_f32_e32 v12, v12, v131
	v_mul_f32_e32 v128, s48, v124
	v_fmac_f32_e32 v13, s80, v124
	v_cvt_f16_f32_e32 v128, v128
	v_cvt_f32_f16_e32 v128, v128
	v_add_f32_e32 v12, v12, v128
	v_mul_f32_e32 v129, s49, v125
	v_fmac_f32_e32 v13, s81, v125
	v_cvt_f16_f32_e32 v129, v129
	v_cvt_f32_f16_e32 v129, v129
	v_add_f32_e32 v12, v12, v129
	v_mul_f32_e32 v130, s50, v126
	v_fmac_f32_e32 v13, s82, v126
	v_cvt_f16_f32_e32 v130, v130
	v_cvt_f32_f16_e32 v130, v130
	v_add_f32_e32 v12, v12, v130
	v_mul_f32_e32 v131, s51, v127
	v_fmac_f32_e32 v13, s83, v127
	v_cvt_f16_f32_e32 v131, v131
	v_cvt_f32_f16_e32 v131, v131
	v_add_f32_e32 v12, v12, v131
	ds_read_b32 v112, v10 offset:12480
	ds_read_b32 v113, v10 offset:12740
	ds_read_b32 v114, v10 offset:13000
	ds_read_b32 v115, v10 offset:13260
	ds_read_b32 v116, v10 offset:13520
	ds_read_b32 v117, v10 offset:13780
	ds_read_b32 v118, v10 offset:14040
	ds_read_b32 v119, v10 offset:14300
	ds_read_b32 v120, v10 offset:14560
	ds_read_b32 v121, v10 offset:14820
	ds_read_b32 v122, v10 offset:15080
	ds_read_b32 v123, v10 offset:15340
	ds_read_b32 v124, v10 offset:15600
	ds_read_b32 v125, v10 offset:15860
	ds_read_b32 v126, v10 offset:16120
	ds_read_b32 v127, v10 offset:16380
	s_waitcnt lgkmcnt(0)
	v_mul_f32_e32 v128, s52, v112
	v_fmac_f32_e32 v13, s84, v112
	v_cvt_f16_f32_e32 v128, v128
	v_cvt_f32_f16_e32 v128, v128
	v_add_f32_e32 v12, v12, v128
	v_mul_f32_e32 v129, s53, v113
	v_fmac_f32_e32 v13, s85, v113
	v_cvt_f16_f32_e32 v129, v129
	v_cvt_f32_f16_e32 v129, v129
	v_add_f32_e32 v12, v12, v129
	v_mul_f32_e32 v130, s54, v114
	v_fmac_f32_e32 v13, s86, v114
	v_cvt_f16_f32_e32 v130, v130
	v_cvt_f32_f16_e32 v130, v130
	v_add_f32_e32 v12, v12, v130
	v_mul_f32_e32 v131, s55, v115
	v_fmac_f32_e32 v13, s87, v115
	v_cvt_f16_f32_e32 v131, v131
	v_cvt_f32_f16_e32 v131, v131
	v_add_f32_e32 v12, v12, v131
	v_mul_f32_e32 v128, s56, v116
	v_fmac_f32_e32 v13, s88, v116
	v_cvt_f16_f32_e32 v128, v128
	v_cvt_f32_f16_e32 v128, v128
	v_add_f32_e32 v12, v12, v128
	v_mul_f32_e32 v129, s57, v117
	v_fmac_f32_e32 v13, s89, v117
	v_cvt_f16_f32_e32 v129, v129
	v_cvt_f32_f16_e32 v129, v129
	v_add_f32_e32 v12, v12, v129
	v_mul_f32_e32 v130, s58, v118
	v_fmac_f32_e32 v13, s90, v118
	v_cvt_f16_f32_e32 v130, v130
	v_cvt_f32_f16_e32 v130, v130
	v_add_f32_e32 v12, v12, v130
	v_mul_f32_e32 v131, s59, v119
	v_fmac_f32_e32 v13, s91, v119
	v_cvt_f16_f32_e32 v131, v131
	v_cvt_f32_f16_e32 v131, v131
	v_add_f32_e32 v12, v12, v131
	v_mul_f32_e32 v128, s60, v120
	v_fmac_f32_e32 v13, s92, v120
	v_cvt_f16_f32_e32 v128, v128
	v_cvt_f32_f16_e32 v128, v128
	v_add_f32_e32 v12, v12, v128
	v_mul_f32_e32 v129, s61, v121
	v_fmac_f32_e32 v13, s93, v121
	v_cvt_f16_f32_e32 v129, v129
	v_cvt_f32_f16_e32 v129, v129
	v_add_f32_e32 v12, v12, v129
	v_mul_f32_e32 v130, s62, v122
	v_fmac_f32_e32 v13, s94, v122
	v_cvt_f16_f32_e32 v130, v130
	v_cvt_f32_f16_e32 v130, v130
	v_add_f32_e32 v12, v12, v130
	v_mul_f32_e32 v131, s63, v123
	v_fmac_f32_e32 v13, s95, v123
	v_cvt_f16_f32_e32 v131, v131
	v_cvt_f32_f16_e32 v131, v131
	v_add_f32_e32 v12, v12, v131
	v_mul_f32_e32 v128, s64, v124
	v_fmac_f32_e32 v13, s96, v124
	v_cvt_f16_f32_e32 v128, v128
	v_cvt_f32_f16_e32 v128, v128
	v_add_f32_e32 v12, v12, v128
	v_mul_f32_e32 v129, s65, v125
	v_fmac_f32_e32 v13, s97, v125
	v_cvt_f16_f32_e32 v129, v129
	v_cvt_f32_f16_e32 v129, v129
	v_add_f32_e32 v12, v12, v129
	v_mul_f32_e32 v130, s66, v126
	v_fmac_f32_e32 v13, s98, v126
	v_cvt_f16_f32_e32 v130, v130
	v_cvt_f32_f16_e32 v130, v130
	v_add_f32_e32 v12, v12, v130
	v_mul_f32_e32 v131, s67, v127
	v_fmac_f32_e32 v13, s99, v127
	v_cvt_f16_f32_e32 v131, v131
	v_cvt_f32_f16_e32 v131, v131
	v_add_f32_e32 v12, v12, v131
	v_lshl_add_u32 v14, v0, 2, 0
	s_lshl_b32 s30, s5, 2
	s_add_u32 s20, s20, s30
	s_addc_u32 s21, s21, 0
	s_add_u32 s22, s22, s30
	s_addc_u32 s23, s23, 0
	global_atomic_add_f32 v14, v12, s[20:21]
	global_atomic_add_f32 v14, v13, s[22:23]

	.amdhsa_kernel _Z6k_attnPKtS0_S0_S0_S0_Pt8PrepArgs
		.amdhsa_group_segment_fixed_size 0
		.amdhsa_private_segment_fixed_size 0
		.amdhsa_kernarg_size 272
		.amdhsa_user_sgpr_count 2
		.amdhsa_user_sgpr_dispatch_ptr 0
		.amdhsa_user_sgpr_queue_ptr 0
		.amdhsa_user_sgpr_kernarg_segment_ptr 1
		.amdhsa_user_sgpr_dispatch_id 0
		.amdhsa_user_sgpr_kernarg_preload_length 0
		.amdhsa_user_sgpr_kernarg_preload_offset 0
		.amdhsa_user_sgpr_private_segment_size 0
		.amdhsa_uses_dynamic_stack 0
		.amdhsa_enable_private_segment 0
		.amdhsa_system_sgpr_workgroup_id_x 1
		.amdhsa_system_sgpr_workgroup_id_y 0
		.amdhsa_system_sgpr_workgroup_id_z 0
		.amdhsa_system_sgpr_workgroup_info 0
		.amdhsa_system_vgpr_workitem_id 0
		.amdhsa_next_free_vgpr 244
		.amdhsa_next_free_sgpr 100
		.amdhsa_accum_offset 244
		.amdhsa_reserve_vcc 1
		.amdhsa_float_round_mode_32 0
		.amdhsa_float_round_mode_16_64 0
		.amdhsa_float_denorm_mode_32 3
		.amdhsa_float_denorm_mode_16_64 3
		.amdhsa_dx10_clamp 1
		.amdhsa_ieee_mode 1
		.amdhsa_fp16_overflow 0
		.amdhsa_tg_split 0
		.amdhsa_exception_fp_ieee_invalid_op 0
		.amdhsa_exception_fp_denorm_src 0
		.amdhsa_exception_fp_ieee_div_zero 0
		.amdhsa_exception_fp_ieee_overflow 0
		.amdhsa_exception_fp_ieee_underflow 0
		.amdhsa_exception_fp_ieee_inexact 0
		.amdhsa_exception_int_div_zero 0
	.end_amdhsa_kernel
